# best + P2 K-loop head padded from 4 mod 8 to 0 mod 8 bytes (compensating pad behind the back edge)
# baseline (speedup 1.0000x reference)
; #define PG8_STAGE(bufoff, gbase, voff) do { _Pragma("unroll") for (int _i = 0; _i < 2; ++_i) \
;         __builtin_amdgcn_global_load_lds((const unsigned*)((const char*)(gbase) + (voff)[_i]), (PG8_LAS unsigned*)(lds + (bufoff) + ldsw + _i * 8192), 16, 0, 0); } while (0)
; #define PG8_LDA(dst, b, h) do { _Pragma("unroll") for (int m = 0; m < 4; ++m) _Pragma("unroll") for (int k = 0; k < 2; ++k) dst[m][k] = *(const PG8_LAS bf16x8*)(lds + PG8_SA(b, h) + aoff + m * 2048 + k * 1024); } while (0)
; #define PG8_LDB(dst, b, h) do { _Pragma("unroll") for (int n = 0; n < 2; ++n) _Pragma("unroll") for (int k = 0; k < 2; ++k) dst[n][k] = *(const PG8_LAS bf16x8*)(lds + PG8_SB(b, h) + boff + n * 2048 + k * 1024); } while (0)
; #define PG8_MMA(ai, bj, At, Bt) do { __builtin_amdgcn_s_setprio(1); _Pragma("unroll") for (int m = 0; m < 4; ++m) _Pragma("unroll") for (int n = 0; n < 2; ++n) _Pragma("unroll") for (int k = 0; k < 2; ++k) \
;         acc[ai][bj][m][n] = __builtin_amdgcn_mfma_f32_16x16x32_bf16(Bt[n][k], At[m][k], acc[ai][bj][m][n], 0, 0, 0); __builtin_amdgcn_s_setprio(0); } while (0)
; #define PG8_BAR __builtin_amdgcn_s_barrier()
; template <class Epi, class Sched, bool ALIGN_EPI = false, bool SP2 = false>
; __device__ __forceinline__ void gemm_phase(PG8_LAS unsigned char* lds, const Gemm g, const Sched& S, const Epi& E) {
;     ...
;         const bool has_next = S.next(ui + 1, nxt);
;         unsigned pend = 0u; if constexpr (Sched::DYNAMIC) pend = S.claim_issue(wid, lane);
;         const char* nA = has_next ? (const char*)(nxt.sel ? g.A2 : g.A) + (size_t)nxt.pm * tstep : cA; const char* nB = has_next ? (const char*)(nxt.sel ? g.Bt2 : g.Bt) + (size_t)nxt.pn * tstep : cB;
;         for (int t = 0; t < nt; t += 2) {
;             const bool last = (t == nt - 2);
;             const char* a1 = cA + (size_t)(t + 1) * kstep;
;             const char* a2 = last ? nA : cA + (size_t)(t + 2) * kstep; const char* b2 = last ? nB : cB + (size_t)(t + 2) * kstep;
;             const char* a3 = a2 + kstep; const char* b3 = b2 + kstep;
;             if (last && has_next) S.a_ready(nxt);
;             if constexpr (SP2) {
;             PG8_LDB(B0, 0, 0); PG8_LDB(B1, 0, 1); PG8_SCHED; PG8_LDA(At, 0, 0); PG8_STAGE(PG8_SA(1, 1), a1 + hstep, voffA);
;             PG8_WAIT_V(8); PG8_WAIT_L(0); PG8_BAR; PG8_MMA(0, 0, At, B0); PG8_MMA(0, 1, At, B1); PG8_BAR; PG8_SCHED;
.LBB0_331:
	s_or_b64 exec, exec, s[0:1]
	s_ashr_i32 s53, s52, 31
	s_lshl_b64 s[0:1], s[52:53], 20
	s_add_u32 s58, s67, s0
	s_addc_u32 s59, s68, s1
	s_and_b64 s[0:1], s[56:57], exec
	s_cselect_b32 s7, s59, s5
	s_cselect_b32 s33, s58, s4
	s_ashr_i32 s55, s54, 31
	s_lshl_b64 s[0:1], s[54:55], 20
	s_add_u32 s60, s69, s0
	s_addc_u32 s61, s70, s1
	s_and_b64 s[0:1], s[56:57], exec
	s_cselect_b32 s53, s61, s3
	s_cselect_b32 s55, s60, s2
	s_add_u32 s0, s4, 0x80080
	s_addc_u32 s1, s5, 0
	s_add_u32 s84, s2, 0x100
	s_addc_u32 s85, s3, 0
	s_mov_b32 s95, -2
	v_mov_b32_e32 v3, v2
	v_mov_b32_e32 v4, v2
	v_mov_b32_e32 v5, v2
	v_mov_b32_e32 v6, v2
	v_mov_b32_e32 v7, v2
	v_mov_b32_e32 v8, v2
	v_mov_b32_e32 v9, v2
	v_mov_b32_e32 v10, v2
	v_mov_b32_e32 v11, v2
	v_mov_b32_e32 v12, v2
	v_mov_b32_e32 v13, v2
	v_mov_b32_e32 v18, v2
	v_mov_b32_e32 v19, v2
	v_mov_b32_e32 v20, v2
	v_mov_b32_e32 v21, v2
	v_mov_b32_e32 v26, v2
	v_mov_b32_e32 v27, v2
	v_mov_b32_e32 v28, v2
	v_mov_b32_e32 v29, v2
	v_mov_b32_e32 v34, v2
	v_mov_b32_e32 v35, v2
	v_mov_b32_e32 v36, v2
	v_mov_b32_e32 v37, v2
	v_mov_b32_e32 v42, v2
	v_mov_b32_e32 v43, v2
	v_mov_b32_e32 v44, v2
	v_mov_b32_e32 v45, v2
	v_mov_b32_e32 v50, v2
	v_mov_b32_e32 v51, v2
	v_mov_b32_e32 v52, v2
	v_mov_b32_e32 v53, v2
	v_mov_b32_e32 v14, v2
	v_mov_b32_e32 v15, v2
	v_mov_b32_e32 v16, v2
	v_mov_b32_e32 v17, v2
	v_mov_b32_e32 v22, v2
	v_mov_b32_e32 v23, v2
	v_mov_b32_e32 v24, v2
	v_mov_b32_e32 v25, v2
	v_mov_b32_e32 v30, v2
	v_mov_b32_e32 v31, v2
	v_mov_b32_e32 v32, v2
	v_mov_b32_e32 v33, v2
	v_mov_b32_e32 v38, v2
	v_mov_b32_e32 v39, v2
	v_mov_b32_e32 v40, v2
	v_mov_b32_e32 v41, v2
	v_mov_b32_e32 v46, v2
	v_mov_b32_e32 v47, v2
	v_mov_b32_e32 v48, v2
	v_mov_b32_e32 v49, v2
	v_mov_b32_e32 v54, v2
	v_mov_b32_e32 v55, v2
	v_mov_b32_e32 v56, v2
	v_mov_b32_e32 v57, v2
	v_mov_b32_e32 v58, v2
	v_mov_b32_e32 v59, v2
	v_mov_b32_e32 v60, v2
	v_mov_b32_e32 v61, v2
	v_mov_b32_e32 v62, v2
	v_mov_b32_e32 v63, v2
	v_mov_b32_e32 v64, v2
	v_mov_b32_e32 v65, v2
	v_mov_b32_e32 v66, v2
	v_mov_b32_e32 v67, v2
	v_mov_b32_e32 v68, v2
	v_mov_b32_e32 v69, v2
	v_mov_b32_e32 v70, v2
	v_mov_b32_e32 v71, v2
	v_mov_b32_e32 v72, v2
	v_mov_b32_e32 v73, v2
	v_mov_b32_e32 v74, v2
	v_mov_b32_e32 v75, v2
	v_mov_b32_e32 v76, v2
	v_mov_b32_e32 v77, v2
	v_mov_b32_e32 v82, v2
	v_mov_b32_e32 v83, v2
	v_mov_b32_e32 v84, v2
	v_mov_b32_e32 v85, v2
	v_mov_b32_e32 v90, v2
	v_mov_b32_e32 v91, v2
	v_mov_b32_e32 v92, v2
	v_mov_b32_e32 v93, v2
	v_mov_b32_e32 v98, v2
	v_mov_b32_e32 v99, v2
	v_mov_b32_e32 v100, v2
	v_mov_b32_e32 v101, v2
	v_mov_b32_e32 v106, v2
	v_mov_b32_e32 v107, v2
	v_mov_b32_e32 v108, v2
	v_mov_b32_e32 v109, v2
	v_mov_b32_e32 v114, v2
	v_mov_b32_e32 v115, v2
	v_mov_b32_e32 v116, v2
	v_mov_b32_e32 v117, v2
	v_mov_b32_e32 v78, v2
	v_mov_b32_e32 v79, v2
	v_mov_b32_e32 v80, v2
	v_mov_b32_e32 v81, v2
	v_mov_b32_e32 v86, v2
	v_mov_b32_e32 v87, v2
	v_mov_b32_e32 v88, v2
	v_mov_b32_e32 v89, v2
	v_mov_b32_e32 v94, v2
	v_mov_b32_e32 v95, v2
	v_mov_b32_e32 v96, v2
	v_mov_b32_e32 v97, v2
	v_mov_b32_e32 v102, v2
	v_mov_b32_e32 v103, v2
	v_mov_b32_e32 v104, v2
	v_mov_b32_e32 v105, v2
	v_mov_b32_e32 v110, v2
	v_mov_b32_e32 v111, v2
	v_mov_b32_e32 v112, v2
	v_mov_b32_e32 v113, v2
	v_mov_b32_e32 v118, v2
	v_mov_b32_e32 v119, v2
	v_mov_b32_e32 v120, v2
	v_mov_b32_e32 v121, v2
	v_mov_b32_e32 v122, v2
	v_mov_b32_e32 v123, v2
	v_mov_b32_e32 v124, v2
	v_mov_b32_e32 v125, v2
	v_mov_b32_e32 v126, v2
	v_mov_b32_e32 v127, v2
	v_mov_b32_e32 v128, v2
	v_mov_b32_e32 v129, v2
	s_nop 0
.LBB0_332:
	ds_read_b128 v[132:135], v213
	ds_read_b128 v[136:139], v213 offset:1024
	ds_read_b128 v[140:143], v213 offset:2048
	ds_read_b128 v[144:147], v213 offset:3072
	ds_read_b128 v[148:151], v214
	ds_read_b128 v[152:155], v214 offset:1024
	ds_read_b128 v[156:159], v214 offset:2048
	ds_read_b128 v[178:181], v214 offset:3072
	s_add_u32 s2, s0, 0xfff80080
	s_addc_u32 s3, s1, -1
	s_cmp_eq_u32 s95, 28
	s_cselect_b32 s5, s7, s3
	s_cselect_b32 s4, s33, s2
	s_cselect_b32 s3, s53, s85
	s_cselect_b32 s2, s55, s84
	v_lshl_add_u64 v[160:161], s[0:1], 0, v[172:173]
	s_add_i32 m0, s63, 0xc000
	ds_read_b128 v[182:185], v215
	ds_read_b128 v[188:191], v215 offset:1024
	ds_read_b128 v[192:195], v215 offset:2048
	ds_read_b128 v[196:199], v215 offset:3072
	ds_read_b128 v[200:203], v215 offset:4096
	ds_read_b128 v[204:207], v215 offset:5120
	ds_read_b128 v[218:221], v215 offset:6144
	ds_read_b128 v[222:225], v215 offset:7168
	global_load_lds_dwordx4 v[160:161], off
	v_lshl_add_u64 v[160:161], s[0:1], 0, v[174:175]
	s_add_i32 m0, s63, 0xe000
	s_nop 0
	global_load_lds_dwordx4 v[160:161], off
	s_waitcnt vmcnt(8)
	s_waitcnt lgkmcnt(0)
	s_barrier
; #define PG8_STAGE(bufoff, gbase, voff) do { _Pragma("unroll") for (int _i = 0; _i < 2; ++_i) \
;         __builtin_amdgcn_global_load_lds((const unsigned*)((const char*)(gbase) + (voff)[_i]), (PG8_LAS unsigned*)(lds + (bufoff) + ldsw + _i * 8192), 16, 0, 0); } while (0)
; #define PG8_LDA(dst, b, h) do { _Pragma("unroll") for (int m = 0; m < 4; ++m) _Pragma("unroll") for (int k = 0; k < 2; ++k) dst[m][k] = *(const PG8_LAS bf16x8*)(lds + PG8_SA(b, h) + aoff + m * 2048 + k * 1024); } while (0)
; #define PG8_MMA(ai, bj, At, Bt) do { __builtin_amdgcn_s_setprio(1); _Pragma("unroll") for (int m = 0; m < 4; ++m) _Pragma("unroll") for (int n = 0; n < 2; ++n) _Pragma("unroll") for (int k = 0; k < 2; ++k) \
;         acc[ai][bj][m][n] = __builtin_amdgcn_mfma_f32_16x16x32_bf16(Bt[n][k], At[m][k], acc[ai][bj][m][n], 0, 0, 0); __builtin_amdgcn_s_setprio(0); } while (0)
; #define PG8_WAIT_V(n) asm volatile("s_waitcnt vmcnt(" #n ")" ::: "memory")
; #define PG8_WAIT_L(n) asm volatile("s_waitcnt lgkmcnt(" #n ")" ::: "memory")
; #define PG8_BAR __builtin_amdgcn_s_barrier()
; #define PG8_SCHED __builtin_amdgcn_sched_barrier(0)
; #define PG8_STAGE(bufoff, gbase, voff) do { _Pragma("unroll") for (int _i = 0; _i < 2; ++_i) \
;         __builtin_amdgcn_global_load_lds((const unsigned*)((const char*)(gbase) + (voff)[_i]), (PG8_LAS unsigned*)(lds + (bufoff) + ldsw + _i * 8192), 16, 0, 0); } while (0)
; #define PG8_LDA(dst, b, h) do { _Pragma("unroll") for (int m = 0; m < 4; ++m) _Pragma("unroll") for (int k = 0; k < 2; ++k) dst[m][k] = *(const PG8_LAS bf16x8*)(lds + PG8_SA(b, h) + aoff + m * 2048 + k * 1024); } while (0)
; #define PG8_WAIT_V(n) asm volatile("s_waitcnt vmcnt(" #n ")" ::: "memory")
; #define PG8_WAIT_L(n) asm volatile("s_waitcnt lgkmcnt(" #n ")" ::: "memory")
; template <class Epi, class Sched, bool ALIGN_EPI = false, bool SP2 = false>
; __device__ __forceinline__ void gemm_phase(PG8_LAS unsigned char* lds, const Gemm g, const Sched& S, const Epi& E) {
;     ...
;             PG8_WAIT_V(8); PG8_WAIT_L(0); PG8_BAR; PG8_MMA(0, 0, At, B0); PG8_MMA(0, 1, At, B1); PG8_BAR; PG8_SCHED;
;             PG8_LDA(At, 0, 1); PG8_STAGE(PG8_SB(0, 0), b2, voffB); PG8_STAGE(PG8_SB(0, 1), b2 + hstep, voffB); PG8_STAGE(PG8_SA(0, 0), a2, voffA);
;             PG8_WAIT_V(8); PG8_WAIT_L(0); PG8_BAR; PG8_MMA(1, 0, At, B0); PG8_MMA(1, 1, At, B1); PG8_BAR; PG8_SCHED;
	s_setprio 1
	s_waitcnt lgkmcnt(0)
	v_mfma_f32_16x16x32_bf16 v[126:129], v[132:135], v[182:185], v[126:129]
	v_mfma_f32_16x16x32_bf16 v[122:125], v[140:143], v[182:185], v[122:125]
	v_mfma_f32_16x16x32_bf16 v[118:121], v[132:135], v[192:195], v[118:121]
	v_mfma_f32_16x16x32_bf16 v[110:113], v[140:143], v[192:195], v[110:113]
	v_mfma_f32_16x16x32_bf16 v[102:105], v[132:135], v[200:203], v[102:105]
	v_mfma_f32_16x16x32_bf16 v[94:97], v[140:143], v[200:203], v[94:97]
	v_mfma_f32_16x16x32_bf16 v[86:89], v[132:135], v[218:221], v[86:89]
	v_mfma_f32_16x16x32_bf16 v[78:81], v[140:143], v[218:221], v[78:81]
	v_mfma_f32_16x16x32_bf16 v[126:129], v[136:139], v[188:191], v[126:129]
	v_mfma_f32_16x16x32_bf16 v[122:125], v[144:147], v[188:191], v[122:125]
	v_mfma_f32_16x16x32_bf16 v[118:121], v[136:139], v[196:199], v[118:121]
	v_mfma_f32_16x16x32_bf16 v[110:113], v[144:147], v[196:199], v[110:113]
	v_mfma_f32_16x16x32_bf16 v[102:105], v[136:139], v[204:207], v[102:105]
	v_mfma_f32_16x16x32_bf16 v[94:97], v[144:147], v[204:207], v[94:97]
	v_mfma_f32_16x16x32_bf16 v[86:89], v[136:139], v[222:225], v[86:89]
	v_mfma_f32_16x16x32_bf16 v[78:81], v[144:147], v[222:225], v[78:81]
	s_setprio 0
	s_setprio 1
	v_mfma_f32_16x16x32_bf16 v[114:117], v[148:151], v[182:185], v[114:117]
	v_mfma_f32_16x16x32_bf16 v[106:109], v[156:159], v[182:185], v[106:109]
	v_mfma_f32_16x16x32_bf16 v[98:101], v[148:151], v[192:195], v[98:101]
	v_mfma_f32_16x16x32_bf16 v[90:93], v[156:159], v[192:195], v[90:93]
	v_mfma_f32_16x16x32_bf16 v[82:85], v[148:151], v[200:203], v[82:85]
	v_mfma_f32_16x16x32_bf16 v[74:77], v[156:159], v[200:203], v[74:77]
	v_mfma_f32_16x16x32_bf16 v[70:73], v[148:151], v[218:221], v[70:73]
	v_mfma_f32_16x16x32_bf16 v[66:69], v[156:159], v[218:221], v[66:69]
	v_mfma_f32_16x16x32_bf16 v[114:117], v[152:155], v[188:191], v[114:117]
	v_mfma_f32_16x16x32_bf16 v[106:109], v[178:181], v[188:191], v[106:109]
	v_mfma_f32_16x16x32_bf16 v[98:101], v[152:155], v[196:199], v[98:101]
	v_mfma_f32_16x16x32_bf16 v[90:93], v[178:181], v[196:199], v[90:93]
	v_mfma_f32_16x16x32_bf16 v[82:85], v[152:155], v[204:207], v[82:85]
	v_mfma_f32_16x16x32_bf16 v[74:77], v[178:181], v[204:207], v[74:77]
	v_mfma_f32_16x16x32_bf16 v[70:73], v[152:155], v[222:225], v[70:73]
	v_mfma_f32_16x16x32_bf16 v[66:69], v[178:181], v[222:225], v[66:69]
	s_setprio 0
	s_barrier
	s_add_i32 s96, s81, s66
	v_lshl_add_u64 v[160:161], s[2:3], 0, v[164:165]
	s_mov_b32 m0, s96
	ds_read_b128 v[182:185], v215 offset:16384
	ds_read_b128 v[188:191], v215 offset:17408
	ds_read_b128 v[192:195], v215 offset:18432
	ds_read_b128 v[196:199], v215 offset:19456
	ds_read_b128 v[200:203], v215 offset:20480
	ds_read_b128 v[204:207], v215 offset:21504
	ds_read_b128 v[218:221], v215 offset:22528
	ds_read_b128 v[222:225], v215 offset:23552
	global_load_lds_dwordx4 v[160:161], off
	s_add_i32 m0, s96, 0x2000
	s_add_u32 s96, s2, 0x80000
	v_lshl_add_u64 v[208:209], s[2:3], 0, v[168:169]
	s_addc_u32 s97, s3, 0
	s_add_i32 vcc_lo, s82, s66
	global_load_lds_dwordx4 v[208:209], off
	v_lshl_add_u64 v[226:227], s[96:97], 0, v[164:165]
	s_mov_b32 m0, vcc_lo
	v_lshl_add_u64 v[228:229], s[4:5], 0, v[166:167]
	global_load_lds_dwordx4 v[226:227], off
	v_lshl_add_u64 v[226:227], s[96:97], 0, v[168:169]
	s_add_i32 m0, vcc_lo, 0x2000
	s_nop 0
	global_load_lds_dwordx4 v[226:227], off
	v_lshl_add_u64 v[226:227], s[4:5], 0, v[162:163]
	s_mov_b32 m0, s63
	s_nop 0
	global_load_lds_dwordx4 v[226:227], off
	s_mov_b32 m0, s65
	s_nop 0
	global_load_lds_dwordx4 v[228:229], off
	s_waitcnt vmcnt(8)
	s_waitcnt lgkmcnt(0)
	s_barrier
	s_setprio 1
	s_waitcnt lgkmcnt(0)
	v_mfma_f32_16x16x32_bf16 v[62:65], v[132:135], v[182:185], v[62:65]
	v_mfma_f32_16x16x32_bf16 v[58:61], v[140:143], v[182:185], v[58:61]
	v_mfma_f32_16x16x32_bf16 v[54:57], v[132:135], v[192:195], v[54:57]
	v_mfma_f32_16x16x32_bf16 v[46:49], v[140:143], v[192:195], v[46:49]
	v_mfma_f32_16x16x32_bf16 v[38:41], v[132:135], v[200:203], v[38:41]
	v_mfma_f32_16x16x32_bf16 v[30:33], v[140:143], v[200:203], v[30:33]
	v_mfma_f32_16x16x32_bf16 v[22:25], v[132:135], v[218:221], v[22:25]
	v_mfma_f32_16x16x32_bf16 v[14:17], v[140:143], v[218:221], v[14:17]
	v_mfma_f32_16x16x32_bf16 v[62:65], v[136:139], v[188:191], v[62:65]
	v_mfma_f32_16x16x32_bf16 v[58:61], v[144:147], v[188:191], v[58:61]
	v_mfma_f32_16x16x32_bf16 v[54:57], v[136:139], v[196:199], v[54:57]
	v_mfma_f32_16x16x32_bf16 v[46:49], v[144:147], v[196:199], v[46:49]
	v_mfma_f32_16x16x32_bf16 v[38:41], v[136:139], v[204:207], v[38:41]
	v_mfma_f32_16x16x32_bf16 v[30:33], v[144:147], v[204:207], v[30:33]
	v_mfma_f32_16x16x32_bf16 v[22:25], v[136:139], v[222:225], v[22:25]
	v_mfma_f32_16x16x32_bf16 v[14:17], v[144:147], v[222:225], v[14:17]
	s_setprio 0
	s_setprio 1
	v_mfma_f32_16x16x32_bf16 v[50:53], v[148:151], v[182:185], v[50:53]
	v_mfma_f32_16x16x32_bf16 v[42:45], v[156:159], v[182:185], v[42:45]
	v_mfma_f32_16x16x32_bf16 v[34:37], v[148:151], v[192:195], v[34:37]
	v_mfma_f32_16x16x32_bf16 v[26:29], v[156:159], v[192:195], v[26:29]
	v_mfma_f32_16x16x32_bf16 v[18:21], v[148:151], v[200:203], v[18:21]
	v_mfma_f32_16x16x32_bf16 v[10:13], v[156:159], v[200:203], v[10:13]
	v_mfma_f32_16x16x32_bf16 v[6:9], v[148:151], v[218:221], v[6:9]
	v_mfma_f32_16x16x32_bf16 v[2:5], v[156:159], v[218:221], v[2:5]
	v_mfma_f32_16x16x32_bf16 v[50:53], v[152:155], v[188:191], v[50:53]
	v_mfma_f32_16x16x32_bf16 v[42:45], v[178:181], v[188:191], v[42:45]
	v_mfma_f32_16x16x32_bf16 v[34:37], v[152:155], v[196:199], v[34:37]
	v_mfma_f32_16x16x32_bf16 v[26:29], v[178:181], v[196:199], v[26:29]
	v_mfma_f32_16x16x32_bf16 v[18:21], v[152:155], v[204:207], v[18:21]
	v_mfma_f32_16x16x32_bf16 v[10:13], v[178:181], v[204:207], v[10:13]
	v_mfma_f32_16x16x32_bf16 v[6:9], v[152:155], v[222:225], v[6:9]
	v_mfma_f32_16x16x32_bf16 v[2:5], v[178:181], v[222:225], v[2:5]
	s_setprio 0
	s_barrier
; #define PG8_STAGE(bufoff, gbase, voff) do { _Pragma("unroll") for (int _i = 0; _i < 2; ++_i) \
;         __builtin_amdgcn_global_load_lds((const unsigned*)((const char*)(gbase) + (voff)[_i]), (PG8_LAS unsigned*)(lds + (bufoff) + ldsw + _i * 8192), 16, 0, 0); } while (0)
; #define PG8_LDA(dst, b, h) do { _Pragma("unroll") for (int m = 0; m < 4; ++m) _Pragma("unroll") for (int k = 0; k < 2; ++k) dst[m][k] = *(const PG8_LAS bf16x8*)(lds + PG8_SA(b, h) + aoff + m * 2048 + k * 1024); } while (0)
; #define PG8_LDB(dst, b, h) do { _Pragma("unroll") for (int n = 0; n < 2; ++n) _Pragma("unroll") for (int k = 0; k < 2; ++k) dst[n][k] = *(const PG8_LAS bf16x8*)(lds + PG8_SB(b, h) + boff + n * 2048 + k * 1024); } while (0)
; #define PG8_MMA(ai, bj, At, Bt) do { __builtin_amdgcn_s_setprio(1); _Pragma("unroll") for (int m = 0; m < 4; ++m) _Pragma("unroll") for (int n = 0; n < 2; ++n) _Pragma("unroll") for (int k = 0; k < 2; ++k) \
;         acc[ai][bj][m][n] = __builtin_amdgcn_mfma_f32_16x16x32_bf16(Bt[n][k], At[m][k], acc[ai][bj][m][n], 0, 0, 0); __builtin_amdgcn_s_setprio(0); } while (0)
; #define PG8_WAIT_V(n) asm volatile("s_waitcnt vmcnt(" #n ")" ::: "memory")
; #define PG8_WAIT_L(n) asm volatile("s_waitcnt lgkmcnt(" #n ")" ::: "memory")
; #define PG8_BAR __builtin_amdgcn_s_barrier()
; #define PG8_SCHED __builtin_amdgcn_sched_barrier(0)
; #define PG8_STAGE(bufoff, gbase, voff) do { _Pragma("unroll") for (int _i = 0; _i < 2; ++_i) \
;         __builtin_amdgcn_global_load_lds((const unsigned*)((const char*)(gbase) + (voff)[_i]), (PG8_LAS unsigned*)(lds + (bufoff) + ldsw + _i * 8192), 16, 0, 0); } while (0)
; #define PG8_LDA(dst, b, h) do { _Pragma("unroll") for (int m = 0; m < 4; ++m) _Pragma("unroll") for (int k = 0; k < 2; ++k) dst[m][k] = *(const PG8_LAS bf16x8*)(lds + PG8_SA(b, h) + aoff + m * 2048 + k * 1024); } while (0)
; #define PG8_WAIT_V(n) asm volatile("s_waitcnt vmcnt(" #n ")" ::: "memory")
; template <class Epi, class Sched, bool ALIGN_EPI = false, bool SP2 = false>
; __device__ __forceinline__ void gemm_phase(PG8_LAS unsigned char* lds, const Gemm g, const Sched& S, const Epi& E) {
;     ...
;             PG8_LDB(B0, 1, 0); PG8_LDB(B1, 1, 1); PG8_SCHED; PG8_LDA(At, 1, 0); PG8_STAGE(PG8_SA(0, 1), a2 + hstep, voffA);
;             PG8_WAIT_V(8); PG8_WAIT_L(0); PG8_BAR; PG8_MMA(0, 0, At, B0); PG8_MMA(0, 1, At, B1); PG8_BAR; PG8_SCHED;
	s_add_i32 s96, 0, 0x18000
	v_add_u32_e32 v131, s96, v211
	s_add_i32 s97, 0, 0x1c000
	ds_read_b128 v[132:135], v131
	ds_read_b128 v[136:139], v131 offset:1024
	ds_read_b128 v[140:143], v131 offset:2048
	ds_read_b128 v[144:147], v131 offset:3072
	v_add_u32_e32 v131, s97, v211
	ds_read_b128 v[148:151], v131
	ds_read_b128 v[152:155], v131 offset:1024
	ds_read_b128 v[156:159], v131 offset:2048
	ds_read_b128 v[178:181], v131 offset:3072
	s_add_u32 s4, s4, 0x80000
	s_addc_u32 s5, s5, 0
	s_mov_b32 m0, s71
	v_lshl_add_u64 v[230:231], s[4:5], 0, v[162:163]
	ds_read_b128 v[182:185], v215 offset:32768
	ds_read_b128 v[188:191], v215 offset:33792
	ds_read_b128 v[192:195], v215 offset:34816
	ds_read_b128 v[196:199], v215 offset:35840
	ds_read_b128 v[200:203], v215 offset:36864
	ds_read_b128 v[204:207], v215 offset:37888
	ds_read_b128 v[218:221], v215 offset:38912
	ds_read_b128 v[222:225], v215 offset:39936
	global_load_lds_dwordx4 v[230:231], off
	v_lshl_add_u64 v[230:231], s[4:5], 0, v[166:167]
	s_mov_b32 m0, s72
	s_nop 0
	global_load_lds_dwordx4 v[230:231], off
	s_waitcnt vmcnt(8)
	s_waitcnt lgkmcnt(0)
	s_barrier
	s_setprio 1
	s_waitcnt lgkmcnt(0)
	v_mfma_f32_16x16x32_bf16 v[126:129], v[132:135], v[182:185], v[126:129]
	v_mfma_f32_16x16x32_bf16 v[122:125], v[140:143], v[182:185], v[122:125]
	v_mfma_f32_16x16x32_bf16 v[118:121], v[132:135], v[192:195], v[118:121]
	v_mfma_f32_16x16x32_bf16 v[110:113], v[140:143], v[192:195], v[110:113]
	v_mfma_f32_16x16x32_bf16 v[102:105], v[132:135], v[200:203], v[102:105]
	v_mfma_f32_16x16x32_bf16 v[94:97], v[140:143], v[200:203], v[94:97]
	v_mfma_f32_16x16x32_bf16 v[86:89], v[132:135], v[218:221], v[86:89]
	v_mfma_f32_16x16x32_bf16 v[78:81], v[140:143], v[218:221], v[78:81]
	v_mfma_f32_16x16x32_bf16 v[126:129], v[136:139], v[188:191], v[126:129]
	v_mfma_f32_16x16x32_bf16 v[122:125], v[144:147], v[188:191], v[122:125]
	v_mfma_f32_16x16x32_bf16 v[118:121], v[136:139], v[196:199], v[118:121]
	v_mfma_f32_16x16x32_bf16 v[110:113], v[144:147], v[196:199], v[110:113]
	v_mfma_f32_16x16x32_bf16 v[102:105], v[136:139], v[204:207], v[102:105]
	v_mfma_f32_16x16x32_bf16 v[94:97], v[144:147], v[204:207], v[94:97]
	v_mfma_f32_16x16x32_bf16 v[86:89], v[136:139], v[222:225], v[86:89]
	v_mfma_f32_16x16x32_bf16 v[78:81], v[144:147], v[222:225], v[78:81]
	s_setprio 0
	s_setprio 1
	v_mfma_f32_16x16x32_bf16 v[114:117], v[148:151], v[182:185], v[114:117]
	v_mfma_f32_16x16x32_bf16 v[106:109], v[156:159], v[182:185], v[106:109]
	v_mfma_f32_16x16x32_bf16 v[98:101], v[148:151], v[192:195], v[98:101]
	v_mfma_f32_16x16x32_bf16 v[90:93], v[156:159], v[192:195], v[90:93]
	v_mfma_f32_16x16x32_bf16 v[82:85], v[148:151], v[200:203], v[82:85]
	v_mfma_f32_16x16x32_bf16 v[74:77], v[156:159], v[200:203], v[74:77]
	v_mfma_f32_16x16x32_bf16 v[70:73], v[148:151], v[218:221], v[70:73]
	v_mfma_f32_16x16x32_bf16 v[66:69], v[156:159], v[218:221], v[66:69]
	v_mfma_f32_16x16x32_bf16 v[114:117], v[152:155], v[188:191], v[114:117]
	v_mfma_f32_16x16x32_bf16 v[106:109], v[178:181], v[188:191], v[106:109]
	v_mfma_f32_16x16x32_bf16 v[98:101], v[152:155], v[196:199], v[98:101]
	v_mfma_f32_16x16x32_bf16 v[90:93], v[178:181], v[196:199], v[90:93]
	v_mfma_f32_16x16x32_bf16 v[82:85], v[152:155], v[204:207], v[82:85]
	v_mfma_f32_16x16x32_bf16 v[74:77], v[178:181], v[204:207], v[74:77]
	v_mfma_f32_16x16x32_bf16 v[70:73], v[152:155], v[222:225], v[70:73]
	v_mfma_f32_16x16x32_bf16 v[66:69], v[178:181], v[222:225], v[66:69]
	s_setprio 0
	s_barrier
; #define PG8_STAGE(bufoff, gbase, voff) do { _Pragma("unroll") for (int _i = 0; _i < 2; ++_i) \
;         __builtin_amdgcn_global_load_lds((const unsigned*)((const char*)(gbase) + (voff)[_i]), (PG8_LAS unsigned*)(lds + (bufoff) + ldsw + _i * 8192), 16, 0, 0); } while (0)
; #define PG8_LDA(dst, b, h) do { _Pragma("unroll") for (int m = 0; m < 4; ++m) _Pragma("unroll") for (int k = 0; k < 2; ++k) dst[m][k] = *(const PG8_LAS bf16x8*)(lds + PG8_SA(b, h) + aoff + m * 2048 + k * 1024); } while (0)
; #define PG8_MMA(ai, bj, At, Bt) do { __builtin_amdgcn_s_setprio(1); _Pragma("unroll") for (int m = 0; m < 4; ++m) _Pragma("unroll") for (int n = 0; n < 2; ++n) _Pragma("unroll") for (int k = 0; k < 2; ++k) \
;         acc[ai][bj][m][n] = __builtin_amdgcn_mfma_f32_16x16x32_bf16(Bt[n][k], At[m][k], acc[ai][bj][m][n], 0, 0, 0); __builtin_amdgcn_s_setprio(0); } while (0)
; #define PG8_WAIT_V(n) asm volatile("s_waitcnt vmcnt(" #n ")" ::: "memory")
; #define PG8_WAIT_L(n) asm volatile("s_waitcnt lgkmcnt(" #n ")" ::: "memory")
; #define PG8_BAR __builtin_amdgcn_s_barrier()
; #define PG8_SCHED __builtin_amdgcn_sched_barrier(0)
; #define PG8_STAGE(bufoff, gbase, voff) do { _Pragma("unroll") for (int _i = 0; _i < 2; ++_i) \
;         __builtin_amdgcn_global_load_lds((const unsigned*)((const char*)(gbase) + (voff)[_i]), (PG8_LAS unsigned*)(lds + (bufoff) + ldsw + _i * 8192), 16, 0, 0); } while (0)
; #define PG8_LDA(dst, b, h) do { _Pragma("unroll") for (int m = 0; m < 4; ++m) _Pragma("unroll") for (int k = 0; k < 2; ++k) dst[m][k] = *(const PG8_LAS bf16x8*)(lds + PG8_SA(b, h) + aoff + m * 2048 + k * 1024); } while (0)
; #define PG8_WAIT_V(n) asm volatile("s_waitcnt vmcnt(" #n ")" ::: "memory")
; template <class Epi, class Sched, bool ALIGN_EPI = false, bool SP2 = false>
; __device__ __forceinline__ void gemm_phase(PG8_LAS unsigned char* lds, const Gemm g, const Sched& S, const Epi& E) {
;     ...
;             PG8_LDA(At, 1, 1); PG8_STAGE(PG8_SB(1, 0), b3, voffB); PG8_STAGE(PG8_SB(1, 1), b3 + hstep, voffB); PG8_STAGE(PG8_SA(1, 0), a3, voffA);
;             PG8_WAIT_V(8); PG8_WAIT_L(0); PG8_BAR; PG8_MMA(1, 0, At, B0); PG8_MMA(1, 1, At, B1); PG8_BAR; PG8_SCHED;
;     ...
;         if constexpr (Sched::DYNAMIC) { static_assert(!Sched::DYNAMIC || ALIGN_EPI, "dynamic orders publish in front of the ALIGN_EPI barrier"); S.claim_publish(ui + 2, pend, wid, lane); }
	s_add_i32 s4, s96, s66
	v_lshl_add_u64 v[160:161], v[160:161], 0, s[40:41]
	s_mov_b32 m0, s4
	ds_read_b128 v[182:185], v215 offset:49152
	ds_read_b128 v[188:191], v215 offset:50176
	ds_read_b128 v[192:195], v215 offset:51200
	ds_read_b128 v[196:199], v215 offset:52224
	ds_read_b128 v[200:203], v215 offset:53248
	ds_read_b128 v[204:207], v215 offset:54272
	ds_read_b128 v[218:221], v215 offset:55296
	ds_read_b128 v[222:225], v215 offset:56320
	global_load_lds_dwordx4 v[160:161], off
	s_add_i32 m0, s4, 0x2000
	s_add_u32 s2, s2, 0x80080
	v_lshl_add_u64 v[160:161], v[208:209], 0, s[40:41]
	s_addc_u32 s3, s3, 0
	s_add_i32 s4, s97, s66
	global_load_lds_dwordx4 v[160:161], off
	v_lshl_add_u64 v[160:161], s[2:3], 0, v[164:165]
	s_mov_b32 m0, s4
	s_nop 0
	global_load_lds_dwordx4 v[160:161], off
	v_lshl_add_u64 v[160:161], s[2:3], 0, v[168:169]
	s_add_i32 m0, s4, 0x2000
	s_nop 0
	global_load_lds_dwordx4 v[160:161], off
	v_lshl_add_u64 v[160:161], v[226:227], 0, s[40:41]
	s_mov_b32 m0, s74
	s_nop 0
	global_load_lds_dwordx4 v[160:161], off
	v_lshl_add_u64 v[160:161], v[228:229], 0, s[40:41]
	s_mov_b32 m0, s75
	s_nop 0
	global_load_lds_dwordx4 v[160:161], off
	s_waitcnt vmcnt(8)
	s_waitcnt lgkmcnt(0)
	s_barrier
	s_setprio 1
	s_waitcnt lgkmcnt(0)
	v_mfma_f32_16x16x32_bf16 v[62:65], v[132:135], v[182:185], v[62:65]
	v_mfma_f32_16x16x32_bf16 v[58:61], v[140:143], v[182:185], v[58:61]
	v_mfma_f32_16x16x32_bf16 v[54:57], v[132:135], v[192:195], v[54:57]
	v_mfma_f32_16x16x32_bf16 v[46:49], v[140:143], v[192:195], v[46:49]
	v_mfma_f32_16x16x32_bf16 v[38:41], v[132:135], v[200:203], v[38:41]
	v_mfma_f32_16x16x32_bf16 v[30:33], v[140:143], v[200:203], v[30:33]
	v_mfma_f32_16x16x32_bf16 v[22:25], v[132:135], v[218:221], v[22:25]
	v_mfma_f32_16x16x32_bf16 v[14:17], v[140:143], v[218:221], v[14:17]
	v_mfma_f32_16x16x32_bf16 v[62:65], v[136:139], v[188:191], v[62:65]
	v_mfma_f32_16x16x32_bf16 v[58:61], v[144:147], v[188:191], v[58:61]
	v_mfma_f32_16x16x32_bf16 v[54:57], v[136:139], v[196:199], v[54:57]
	v_mfma_f32_16x16x32_bf16 v[46:49], v[144:147], v[196:199], v[46:49]
	v_mfma_f32_16x16x32_bf16 v[38:41], v[136:139], v[204:207], v[38:41]
	v_mfma_f32_16x16x32_bf16 v[30:33], v[144:147], v[204:207], v[30:33]
	v_mfma_f32_16x16x32_bf16 v[22:25], v[136:139], v[222:225], v[22:25]
	v_mfma_f32_16x16x32_bf16 v[14:17], v[144:147], v[222:225], v[14:17]
	s_setprio 0
	s_setprio 1
	v_mfma_f32_16x16x32_bf16 v[50:53], v[148:151], v[182:185], v[50:53]
	v_mfma_f32_16x16x32_bf16 v[42:45], v[156:159], v[182:185], v[42:45]
	v_mfma_f32_16x16x32_bf16 v[34:37], v[148:151], v[192:195], v[34:37]
	v_mfma_f32_16x16x32_bf16 v[26:29], v[156:159], v[192:195], v[26:29]
	v_mfma_f32_16x16x32_bf16 v[18:21], v[148:151], v[200:203], v[18:21]
	v_mfma_f32_16x16x32_bf16 v[10:13], v[156:159], v[200:203], v[10:13]
	v_mfma_f32_16x16x32_bf16 v[6:9], v[148:151], v[218:221], v[6:9]
	v_mfma_f32_16x16x32_bf16 v[2:5], v[156:159], v[218:221], v[2:5]
	v_mfma_f32_16x16x32_bf16 v[50:53], v[152:155], v[188:191], v[50:53]
	v_mfma_f32_16x16x32_bf16 v[42:45], v[178:181], v[188:191], v[42:45]
	v_mfma_f32_16x16x32_bf16 v[34:37], v[152:155], v[196:199], v[34:37]
	v_mfma_f32_16x16x32_bf16 v[26:29], v[178:181], v[196:199], v[26:29]
	v_mfma_f32_16x16x32_bf16 v[18:21], v[152:155], v[204:207], v[18:21]
	v_mfma_f32_16x16x32_bf16 v[10:13], v[178:181], v[204:207], v[10:13]
	v_mfma_f32_16x16x32_bf16 v[6:9], v[152:155], v[222:225], v[6:9]
	v_mfma_f32_16x16x32_bf16 v[2:5], v[178:181], v[222:225], v[2:5]
	s_setprio 0
	s_barrier
	s_add_i32 s95, s95, 2
	s_add_u32 s0, s0, 0x100
	s_addc_u32 s1, s1, 0
	s_add_u32 s84, s84, 0x100
	s_addc_u32 s85, s85, 0
	s_cmp_gt_u32 s95, 29
	s_cbranch_scc0 .LBB0_332
	s_nop 0
	s_waitcnt vmcnt(0)
	v_readfirstlane_b32 s2, v130
	s_and_saveexec_b64 s[0:1], s[10:11]
	s_cbranch_execz .LBB0_335
	s_and_b32 s3, s6, 3
	s_xor_b32 s3, s3, 2
	s_and_b64 s[4:5], s[42:43], exec
	s_cselect_b32 s3, s3, s76
	s_lshl_b32 s3, s3, 2
	s_add_i32 s3, s3, 0
	s_add_i32 s3, s3, 0x27da0
	v_mov_b32_e32 v130, s3
	v_mov_b32_e32 v131, s2
	ds_write_b32 v130, v131
